# chained MoE: list index -> workgroup mapping permuted so each XCD takes 4 consecutive row tiles x all 8 column tiles (a gathered activation tile is fetched into one XCD's L2 and shared by 8 workgroups
# baseline (speedup 1.0000x reference)
.LBB0_1823:
	s_or_b64 exec, exec, s[4:5]
	s_add_u32 s54, s40, 0x10000
	s_addc_u32 s55, s41, 0
	s_add_u32 s24, s0, 0xf8
	s_addc_u32 s25, s1, 0
	s_add_i32 s4, 0, 0x20080
	v_mov_b32_e32 v1, s4
	s_waitcnt lgkmcnt(0)
	s_barrier
	ds_read_b32 v2, v1
	s_load_dword s33, s[0:1], 0xf8
	s_add_u32 s26, s40, 0x300000
	s_addc_u32 s27, s41, 0
	s_add_u32 s12, s40, 0x36600000
	s_waitcnt lgkmcnt(0)
	v_readfirstlane_b32 s35, v2
	v_mov_b32 v2, v0
	ds_read_b32 v1, v1
	s_addc_u32 s4, s41, 0
	s_mov_b32 s97, s2
	s_cmp_lg_u32 s33, 0x100
	s_cbranch_scc1 .Lmoe_perm_done_0
	s_and_b32 s97, s2, 7
	s_lshl_b32 s97, s97, 5
	s_lshr_b32 s98, s2, 6
	s_lshl_b32 s98, s98, 3
	s_or_b32 s97, s97, s98
	s_bfe_u32 s98, s2, 0x30003
	s_or_b32 s97, s97, s98
.Lmoe_perm_done_0:
	s_and_b32 s13, s4, 0xffff
	s_mov_b32 s15, 0x20000
	s_brev_b32 s14, -2
	s_waitcnt lgkmcnt(0)
	v_lshlrev_b32_e32 v1, 3, v1
	v_cmp_ge_i32_e32 vcc, s97, v1
	v_readfirstlane_b32 s6, v2
	s_cbranch_vccnz .LBB0_1882
	v_ashrrev_i32_e32 v1, 31, v2
	v_lshrrev_b32_e32 v1, 26, v1
	v_add_u32_e32 v1, v2, v1
	s_waitcnt vmcnt(5)
	v_ashrrev_i32_e32 v12, 6, v1
	v_bfe_i32 v1, v2, 27, 1
	s_waitcnt vmcnt(0)
	v_lshlrev_b32_e32 v3, 4, v2
	v_lshrrev_b32_e32 v1, 22, v1
	v_add_u32_e32 v1, v3, v1
	v_and_b32_e32 v1, 0xfffffc00, v1
	v_sub_u32_e32 v1, v3, v1
	v_lshrrev_b32_e32 v4, 4, v1
	v_bitop3_b32 v13, v4, v1, 32 bitop3:0x6c
	v_ashrrev_i32_e32 v1, 31, v1
	v_lshrrev_b32_e32 v1, 26, v1
	v_lshlrev_b32_e32 v4, 3, v12
	v_add_u32_e32 v1, v13, v1
	v_and_b32_e32 v4, -16, v4
	v_ashrrev_i32_e32 v14, 6, v1
	v_add_u32_e32 v3, 0x2000, v3
	v_add_u32_e32 v1, v14, v4
	v_ashrrev_i32_e32 v4, 31, v3
	v_lshrrev_b32_e32 v4, 22, v4
	v_add_u32_e32 v4, v3, v4
	v_ashrrev_i32_e32 v15, 10, v4
	v_mul_i32_i24_e32 v4, 0x400, v15
	v_sub_u32_e32 v3, v3, v4
	s_add_u32 s16, s40, 0x9c00000
	v_lshrrev_b32_e32 v4, 4, v3
	s_addc_u32 s4, s41, 0
	v_bitop3_b32 v3, v4, v3, 32 bitop3:0x6c
	v_lshlrev_b32_e32 v4, 3, v15
	s_add_u32 s20, s40, 0x4dd00000
	v_and_b32_e32 v16, -16, v4
	v_ashrrev_i32_e32 v4, 31, v3
	s_addc_u32 s5, s41, 0
	v_lshrrev_b32_e32 v4, 26, v4
	s_add_i32 s7, 0, 0x20044
	v_add_u32_e32 v17, v3, v4
	v_mov_b32_e32 v4, s7
	ds_read2_b32 v[4:5], v4 offset1:1
	s_add_i32 s7, 0, 0x2004c
	v_mov_b32_e32 v6, s7
	s_add_i32 s7, 0, 0x20054
	v_mov_b32_e32 v8, s7
	s_add_i32 s7, 0, 0x2005c
	v_mov_b32_e32 v10, s7
	s_ashr_i32 s46, s97, 3
	ds_read2_b32 v[6:7], v6 offset1:1
	ds_read2_b32 v[8:9], v8 offset1:1
	ds_read2_b32 v[10:11], v10 offset1:1
	s_waitcnt lgkmcnt(3)
	v_cmp_ge_i32_e32 vcc, s46, v4
	s_add_i32 s7, 0, 0x20064
	v_add_u32_e32 v197, 0x80, v1
	v_cndmask_b32_e64 v4, 0, 1, vcc
	v_cmp_lt_i32_e32 vcc, s46, v5
	s_mov_b32 s8, 0x1fffe0
	s_and_b32 s17, s4, 0xffff
	v_cndmask_b32_e32 v4, 2, v4, vcc
	s_waitcnt lgkmcnt(2)
	v_cmp_lt_i32_e32 vcc, s46, v6
	s_and_b32 s38, s97, 7
	s_and_b32 s21, s5, 0xffff
	v_cndmask_b32_e32 v4, 3, v4, vcc
	v_cmp_lt_i32_e32 vcc, s46, v7
	s_lshl_b32 s5, s38, 19
	s_mov_b32 s22, s14
	v_cndmask_b32_e32 v4, 4, v4, vcc
	s_waitcnt lgkmcnt(1)
	v_cmp_lt_i32_e32 vcc, s46, v8
	s_mov_b32 s23, s15
	s_mov_b32 s18, s14
	v_cndmask_b32_e32 v4, 5, v4, vcc
	v_cmp_lt_i32_e32 vcc, s46, v9
	s_mov_b32 s19, s15
	s_nop 0
	v_cndmask_b32_e32 v4, 6, v4, vcc
	s_waitcnt lgkmcnt(0)
	v_cmp_lt_i32_e32 vcc, s46, v10
	s_nop 1
	v_cndmask_b32_e32 v4, 7, v4, vcc
	v_cmp_lt_i32_e32 vcc, s46, v11
	s_nop 1
	v_cndmask_b32_e32 v10, 8, v4, vcc
	v_mov_b32_e32 v4, s7
	ds_read2_b32 v[4:5], v4 offset1:1
	s_add_i32 s7, 0, 0x2006c
	v_mov_b32_e32 v6, s7
	s_add_i32 s7, 0, 0x20074
	v_mov_b32_e32 v8, s7
	s_add_i32 s7, 0, 0x2007c
	v_mov_b32_e32 v11, s7
	ds_read2_b32 v[6:7], v6 offset1:1
	ds_read2_b32 v[8:9], v8 offset1:1
	ds_read_b32 v11, v11
	s_waitcnt lgkmcnt(3)
	v_cmp_lt_i32_e32 vcc, s46, v4
	s_movk_i32 s7, 0x4200
	s_nop 0
	v_cndmask_b32_e32 v4, 9, v10, vcc
	v_cmp_lt_i32_e32 vcc, s46, v5
	v_ashrrev_i32_e32 v10, 6, v17
	v_add_u32_e32 v196, v10, v16
	v_cndmask_b32_e32 v4, 10, v4, vcc
	s_waitcnt lgkmcnt(2)
	v_cmp_lt_i32_e32 vcc, s46, v6
	v_add_u32_e32 v198, 0x80, v196
	s_nop 0
	v_cndmask_b32_e32 v4, 11, v4, vcc
	v_cmp_lt_i32_e32 vcc, s46, v7
	s_nop 1
	v_cndmask_b32_e32 v4, 12, v4, vcc
	s_waitcnt lgkmcnt(1)
	v_cmp_lt_i32_e32 vcc, s46, v8
	s_nop 1
	v_cndmask_b32_e32 v4, 13, v4, vcc
	v_cmp_lt_i32_e32 vcc, s46, v9
	s_nop 1
	v_cndmask_b32_e32 v4, 14, v4, vcc
	s_waitcnt lgkmcnt(0)
	v_cmp_lt_i32_e32 vcc, s46, v11
	s_nop 1
	v_cndmask_b32_e32 v194, 15, v4, vcc
	v_lshlrev_b32_e32 v4, 2, v194
	v_add_u32_e32 v4, 0, v4
	v_add_u32_e32 v4, 0x20000, v4
	ds_read2_b32 v[4:5], v4 offset1:16
	v_mul_lo_u32 v11, v194, s7
	s_ashr_i32 s7, s6, 8
	s_waitcnt lgkmcnt(0)
	v_sub_u32_e32 v5, s46, v5
	v_lshlrev_b32_e32 v16, 8, v5
	v_add_u32_e32 v5, v16, v1
	v_add_u32_e32 v18, -1, v4
	v_min_i32_e32 v4, v5, v18
	v_add_u32_e32 v6, v16, v197
	v_add_u32_e32 v8, v16, v196
	v_add_u32_e32 v4, v4, v11
	v_min_i32_e32 v6, v6, v18
	v_min_i32_e32 v8, v8, v18
	v_ashrrev_i32_e32 v5, 31, v4
	v_add_u32_e32 v6, v6, v11
	v_add_u32_e32 v8, v8, v11
	v_lshl_add_u64 v[4:5], v[4:5], 2, s[26:27]
	v_ashrrev_i32_e32 v7, 31, v6
	v_ashrrev_i32_e32 v9, 31, v8
	v_lshl_add_u64 v[6:7], v[6:7], 2, s[26:27]
	v_lshl_add_u64 v[8:9], v[8:9], 2, s[26:27]
	global_load_dword v19, v[4:5], off
	global_load_dword v20, v[6:7], off
	global_load_dword v21, v[8:9], off
	v_add_u32_e32 v4, v16, v198
	v_min_i32_e32 v4, v4, v18
	v_add_u32_e32 v4, v4, v11
	v_ashrrev_i32_e32 v5, 31, v4
	v_lshl_add_u64 v[4:5], v[4:5], 2, s[26:27]
	global_load_dword v4, v[4:5], off
	v_mul_i32_i24_e32 v6, 64, v14
	v_sub_u32_e32 v6, v13, v6
	v_mov_b32_e32 v7, 1
	v_lshlrev_b32_e32 v5, 5, v12
	v_ashrrev_i16_sdwa v6, v7, sext(v6) dst_sel:DWORD dst_unused:UNUSED_PAD src0_sel:DWORD src1_sel:BYTE_0
	v_and_b32_e32 v5, 32, v5
	v_bfe_i32 v6, v6, 0, 16
	v_add_lshl_u32 v199, v5, v6, 1
	v_and_b32_e32 v6, 0xc0, v17
	v_sub_u32_e32 v3, v3, v6
	v_lshlrev_b32_e32 v5, 5, v15
	v_ashrrev_i16_sdwa v3, v7, sext(v3) dst_sel:DWORD dst_unused:UNUSED_PAD src0_sel:DWORD src1_sel:BYTE_0
	v_and_b32_e32 v5, 32, v5
	v_bfe_i32 v3, v3, 0, 16
	v_add_lshl_u32 v201, v5, v3, 1
	v_lshlrev_b32_e32 v8, 1, v1
	v_lshrrev_b32_e32 v9, 2, v1
	v_and_b32_e32 v11, 3, v14
	v_and_b32_e32 v8, 24, v8
	v_and_b32_e32 v9, 4, v9
	v_and_or_b32 v11, v1, s8, v11
	v_or3_b32 v8, v11, v9, v8
	v_lshl_add_u32 v200, v8, 11, v199
	v_and_b32_e32 v8, 3, v10
	v_lshlrev_b32_e32 v6, 1, v196
	v_lshrrev_b32_e32 v7, 2, v196
	v_and_or_b32 v8, v196, s8, v8
	s_ashr_i32 s8, s6, 6
	v_and_b32_e32 v6, 24, v6
	v_and_b32_e32 v7, 4, v7
	s_lshl_b32 s4, s8, 10
	v_or3_b32 v6, v8, v7, v6
	s_add_i32 s47, s4, 0
	v_lshl_add_u32 v202, v6, 11, v201
	s_add_i32 s48, s47, 0x10000
	s_mov_b32 m0, s48
	s_waitcnt vmcnt(3)
	v_lshlrev_b32_e32 v3, 10, v19
	v_and_b32_e32 v3, 0xfffff800, v3
	v_add_u32_e32 v195, v3, v199
	s_waitcnt vmcnt(2)
	v_lshlrev_b32_e32 v3, 10, v20
	v_and_b32_e32 v3, 0xfffff800, v3
	v_add_u32_e32 v218, v3, v199
	s_waitcnt vmcnt(1)
	v_lshlrev_b32_e32 v3, 10, v21
	v_and_b32_e32 v3, 0xfffff800, v3
	v_add_u32_e32 v217, v3, v201
	s_waitcnt vmcnt(0)
	v_lshlrev_b32_e32 v3, 10, v4
	v_and_b32_e32 v3, 0xfffff800, v3
	v_add_u32_e32 v219, v3, v201
	v_lshlrev_b32_e32 v3, 22, v194
	v_or_b32_e32 v220, s5, v3
	s_mov_b64 s[4:5], exec
	v_readfirstlane_b32 s9, v220
	s_nop 4
	buffer_load_dwordx4 v200, s[16:19], s9 offen lds
	s_mov_b64 exec, s[4:5]
	s_add_i32 s49, s47, 0x12000
	s_mov_b64 s[4:5], exec
	s_mov_b32 m0, s49
	s_nop 0
	buffer_load_dwordx4 v202, s[16:19], s9 offen lds
	s_mov_b64 exec, s[4:5]
	s_add_i32 s50, s47, 0x14000
	v_or_b32_e32 v3, 0x40000, v220
	s_mov_b64 s[4:5], exec
	s_mov_b32 m0, s50
	v_readfirstlane_b32 s9, v3
	s_nop 4
	buffer_load_dwordx4 v200, s[16:19], s9 offen lds
	s_mov_b64 exec, s[4:5]
	s_add_i32 s51, s47, 0x16000
	s_mov_b64 s[4:5], exec
	s_mov_b32 m0, s51
	s_nop 0
	buffer_load_dwordx4 v202, s[16:19], s9 offen lds
	s_mov_b64 exec, s[4:5]
	s_mov_b32 m0, s47
	s_add_i32 s52, s47, 0x2000
	buffer_load_dwordx4 v195, s[20:23], 0 offen lds
	s_mov_b32 m0, s52
	s_add_i32 s53, s47, 0x4000
	buffer_load_dwordx4 v217, s[20:23], 0 offen lds
	s_mov_b32 m0, s53
	s_add_i32 s56, s47, 0x6000
	buffer_load_dwordx4 v218, s[20:23], 0 offen lds
	s_mov_b32 m0, s56
	s_cmp_eq_u32 s7, 1
	buffer_load_dwordx4 v219, s[20:23], 0 offen lds
	s_cselect_b64 s[10:11], -1, 0
	s_cmp_lg_u32 s7, 1
	s_cbranch_scc1 .LBB0_1834
	s_barrier

.LBB0_1845:
	ds_read_b32 v2, v205
	s_add_i32 s64, s64, 1
	s_mul_i32 s6, s64, s33
	s_add_i32 s6, s6, s97
	s_waitcnt lgkmcnt(0)
	v_lshlrev_b32_e32 v2, 3, v2
	v_cmp_ge_i32_e32 vcc, s6, v2
	v_cmp_lt_i32_e64 s[8:9], s6, v2
	s_cbranch_vccnz .LBB0_1847
	v_mov_b32_e32 v2, s67
	ds_read2_b32 v[2:3], v2 offset1:1
	v_mov_b32_e32 v4, s68
	v_mov_b32_e32 v6, s69
	v_mov_b32_e32 v8, s70
	s_ashr_i32 s76, s6, 3
	ds_read2_b32 v[4:5], v4 offset1:1
	ds_read2_b32 v[6:7], v6 offset1:1
	ds_read2_b32 v[8:9], v8 offset1:1
	s_waitcnt lgkmcnt(3)
	v_cmp_ge_i32_e32 vcc, s76, v2
	s_and_b32 s77, s6, 7
	s_nop 0
	v_cndmask_b32_e64 v2, 0, 1, vcc
	v_cmp_lt_i32_e32 vcc, s76, v3
	s_nop 1
	v_cndmask_b32_e32 v2, 2, v2, vcc
	s_waitcnt lgkmcnt(2)
	v_cmp_lt_i32_e32 vcc, s76, v4
	v_mov_b32_e32 v4, s72
	s_nop 0
	v_cndmask_b32_e32 v2, 3, v2, vcc
	v_cmp_lt_i32_e32 vcc, s76, v5
	s_nop 1
	v_cndmask_b32_e32 v2, 4, v2, vcc
	s_waitcnt lgkmcnt(1)
	v_cmp_lt_i32_e32 vcc, s76, v6
	v_mov_b32_e32 v6, s73
	s_nop 0
	v_cndmask_b32_e32 v2, 5, v2, vcc
	v_cmp_lt_i32_e32 vcc, s76, v7
	s_nop 1
	v_cndmask_b32_e32 v2, 6, v2, vcc
	s_waitcnt lgkmcnt(0)
	v_cmp_lt_i32_e32 vcc, s76, v8
	s_nop 1
	v_cndmask_b32_e32 v2, 7, v2, vcc
	v_cmp_lt_i32_e32 vcc, s76, v9
	v_mov_b32_e32 v9, s74
	s_nop 0
	v_cndmask_b32_e32 v8, 8, v2, vcc
	v_mov_b32_e32 v2, s71
	ds_read2_b32 v[2:3], v2 offset1:1
	ds_read2_b32 v[4:5], v4 offset1:1
	ds_read2_b32 v[6:7], v6 offset1:1
	ds_read_b32 v9, v9
	s_waitcnt lgkmcnt(3)
	v_cmp_lt_i32_e32 vcc, s76, v2
	s_nop 1
	v_cndmask_b32_e32 v2, 9, v8, vcc
	v_cmp_lt_i32_e32 vcc, s76, v3
	s_nop 1
	v_cndmask_b32_e32 v2, 10, v2, vcc
	s_waitcnt lgkmcnt(2)
	v_cmp_lt_i32_e32 vcc, s76, v4
	s_nop 1
	v_cndmask_b32_e32 v2, 11, v2, vcc
	v_cmp_lt_i32_e32 vcc, s76, v5
	s_nop 1
	v_cndmask_b32_e32 v2, 12, v2, vcc
	s_waitcnt lgkmcnt(1)
	v_cmp_lt_i32_e32 vcc, s76, v6
	s_nop 1
	v_cndmask_b32_e32 v2, 13, v2, vcc
	v_cmp_lt_i32_e32 vcc, s76, v7
	s_nop 1
	v_cndmask_b32_e32 v2, 14, v2, vcc
	s_waitcnt lgkmcnt(0)
	v_cmp_lt_i32_e32 vcc, s76, v9
	s_nop 1
	v_cndmask_b32_e32 v211, 15, v2, vcc

.LBB0_1882:
	s_lshl_b32 s56, s35, 3
	s_cmp_le_i32 s56, s97
	s_mov_b32 s57, 0
	s_cbranch_scc1 .LBB0_1884
	s_abs_i32 s4, s33
	v_cvt_f32_u32_e32 v1, s4
	s_not_b32 s5, s97
	s_sub_i32 s6, 0, s4
	s_add_i32 s5, s33, s5
	v_rcp_iflag_f32_e32 v1, v1
	s_add_i32 s5, s5, s56
	s_xor_b32 s7, s5, s33
	s_abs_i32 s5, s5
	v_mul_f32_e32 v1, 0x4f7ffffe, v1
	v_cvt_u32_f32_e32 v1, v1
	s_ashr_i32 s7, s7, 31
	v_readfirstlane_b32 s8, v1
	s_mul_i32 s6, s6, s8
	s_mul_hi_u32 s6, s8, s6
	s_add_i32 s8, s8, s6
	s_mul_hi_u32 s6, s5, s8
	s_mul_i32 s8, s6, s4
	s_sub_i32 s5, s5, s8
	s_add_i32 s9, s6, 1
	s_sub_i32 s8, s5, s4
	s_cmp_ge_u32 s5, s4
	s_cselect_b32 s6, s9, s6
	s_cselect_b32 s5, s8, s5
	s_add_i32 s8, s6, 1
	s_cmp_ge_u32 s5, s4
	s_cselect_b32 s4, s8, s6
	s_xor_b32 s4, s4, s7
	s_sub_i32 s57, s4, s7
.LBB0_1884:
	s_add_i32 s4, 0, 0x20080
	s_movk_i32 s30, 0x400
	v_mov_b32_e32 v1, s4
	v_mov_b32 v2, v0
	ds_read_b32 v1, v1
	s_mul_i32 s6, s57, s33
	s_add_i32 s6, s6, s97
	s_sub_i32 s7, s6, s56
	v_readfirstlane_b32 s31, v2
	s_waitcnt lgkmcnt(0)
	v_lshlrev_b32_e32 v1, 3, v1
	v_cmp_ge_i32_e32 vcc, s7, v1
	v_cmp_lt_i32_e64 s[4:5], s7, v1
	s_cbranch_vccnz .LBB0_1886
	s_ashr_i32 s34, s7, 3
	s_add_i32 s7, 0, 0x20044
	v_mov_b32_e32 v1, s7
	ds_read2_b32 v[4:5], v1 offset1:1
	s_add_i32 s7, 0, 0x2004c
	v_mov_b32_e32 v1, s7
	s_add_i32 s7, 0, 0x20054
	s_waitcnt vmcnt(0)
	v_mov_b32_e32 v3, s7
	s_add_i32 s7, 0, 0x2005c
	v_mov_b32_e32 v10, s7
	ds_read2_b32 v[6:7], v1 offset1:1
	ds_read2_b32 v[8:9], v3 offset1:1
	ds_read2_b32 v[10:11], v10 offset1:1
	s_waitcnt lgkmcnt(3)
	v_cmp_ge_i32_e32 vcc, s34, v4
	s_add_i32 s7, 0, 0x20064
	v_mov_b32_e32 v3, s7
	v_cndmask_b32_e64 v1, 0, 1, vcc
	v_cmp_lt_i32_e32 vcc, s34, v5
	ds_read2_b32 v[4:5], v3 offset1:1
	s_add_i32 s7, 0, 0x2006c
	v_cndmask_b32_e32 v1, 2, v1, vcc
	s_waitcnt lgkmcnt(3)
	v_cmp_lt_i32_e32 vcc, s34, v6
	v_mov_b32_e32 v3, s7
	s_add_i32 s7, 0, 0x20074
	v_cndmask_b32_e32 v1, 3, v1, vcc
	v_cmp_lt_i32_e32 vcc, s34, v7
	s_and_b32 s58, s6, 7
	s_nop 0
	v_cndmask_b32_e32 v1, 4, v1, vcc
	s_waitcnt lgkmcnt(2)
	v_cmp_lt_i32_e32 vcc, s34, v8
	v_mov_b32_e32 v8, s7
	s_add_i32 s7, 0, 0x2007c
	v_cndmask_b32_e32 v1, 5, v1, vcc
	v_cmp_lt_i32_e32 vcc, s34, v9
	s_nop 1
	v_cndmask_b32_e32 v1, 6, v1, vcc
	s_waitcnt lgkmcnt(1)
	v_cmp_lt_i32_e32 vcc, s34, v10
	v_mov_b32_e32 v10, s7
	ds_read2_b32 v[6:7], v3 offset1:1
	ds_read2_b32 v[8:9], v8 offset1:1
	ds_read_b32 v3, v10
	v_cndmask_b32_e32 v1, 7, v1, vcc
	v_cmp_lt_i32_e32 vcc, s34, v11
	s_nop 1
	v_cndmask_b32_e32 v1, 8, v1, vcc
	s_waitcnt lgkmcnt(3)
	v_cmp_lt_i32_e32 vcc, s34, v4
	s_nop 1
	v_cndmask_b32_e32 v1, 9, v1, vcc
	v_cmp_lt_i32_e32 vcc, s34, v5
	s_nop 1
	v_cndmask_b32_e32 v1, 10, v1, vcc
	s_waitcnt lgkmcnt(2)
	v_cmp_lt_i32_e32 vcc, s34, v6
	s_nop 1
	v_cndmask_b32_e32 v1, 11, v1, vcc
	v_cmp_lt_i32_e32 vcc, s34, v7
	s_nop 1
	v_cndmask_b32_e32 v1, 12, v1, vcc
	s_waitcnt lgkmcnt(1)
	v_cmp_lt_i32_e32 vcc, s34, v8
	s_nop 1
	v_cndmask_b32_e32 v1, 13, v1, vcc
	v_cmp_lt_i32_e32 vcc, s34, v9
	s_nop 1
	v_cndmask_b32_e32 v1, 14, v1, vcc
	s_waitcnt lgkmcnt(0)
	v_cmp_lt_i32_e32 vcc, s34, v3
	s_nop 1
	v_cndmask_b32_e32 v208, 15, v1, vcc
	v_lshlrev_b32_e32 v1, 2, v208
	v_add_u32_e32 v1, 0, v1
	v_add_u32_e32 v1, 0x20000, v1
	ds_read2_b32 v[4:5], v1 offset1:16
	s_waitcnt lgkmcnt(0)
	v_subrev_u32_e32 v1, s34, v5
	v_lshlrev_b32_e32 v1, 8, v1
	v_add_u32_e32 v1, v1, v4
	s_andn2_b64 vcc, exec, s[4:5]
	s_cbranch_vccz .LBB0_1887
	s_branch .LBB0_1983

.LBB0_1923:
	ds_read_b32 v2, v200
	s_add_i32 s89, s89, 1
	s_add_i32 s8, s89, s57
	s_mul_i32 s10, s8, s33
	s_add_i32 s10, s10, s97
	s_sub_i32 s11, s10, s56
	s_waitcnt lgkmcnt(0)
	v_lshlrev_b32_e32 v2, 3, v2
	v_cmp_ge_i32_e32 vcc, s11, v2
	v_cmp_lt_i32_e64 s[8:9], s11, v2
	s_cbranch_vccnz .LBB0_1925
	v_mov_b32_e32 v2, s79
	ds_read2_b32 v[2:3], v2 offset1:1
	v_mov_b32_e32 v4, s80
	v_mov_b32_e32 v6, s81
	v_mov_b32_e32 v8, s82
	s_ashr_i32 s88, s11, 3
	ds_read2_b32 v[4:5], v4 offset1:1
	ds_read2_b32 v[6:7], v6 offset1:1
	ds_read2_b32 v[8:9], v8 offset1:1
	s_waitcnt lgkmcnt(3)
	v_cmp_ge_i32_e32 vcc, s88, v2
	s_and_b32 s90, s10, 7
	s_nop 0
	v_cndmask_b32_e64 v2, 0, 1, vcc
	v_cmp_lt_i32_e32 vcc, s88, v3
	s_nop 1
	v_cndmask_b32_e32 v2, 2, v2, vcc
	s_waitcnt lgkmcnt(2)
	v_cmp_lt_i32_e32 vcc, s88, v4
	v_mov_b32_e32 v4, s84
	s_nop 0
	v_cndmask_b32_e32 v2, 3, v2, vcc
	v_cmp_lt_i32_e32 vcc, s88, v5
	s_nop 1
	v_cndmask_b32_e32 v2, 4, v2, vcc
	s_waitcnt lgkmcnt(1)
	v_cmp_lt_i32_e32 vcc, s88, v6
	v_mov_b32_e32 v6, s85
	s_nop 0
	v_cndmask_b32_e32 v2, 5, v2, vcc
	v_cmp_lt_i32_e32 vcc, s88, v7
	s_nop 1
	v_cndmask_b32_e32 v2, 6, v2, vcc
	s_waitcnt lgkmcnt(0)
	v_cmp_lt_i32_e32 vcc, s88, v8
	s_nop 1
	v_cndmask_b32_e32 v2, 7, v2, vcc
	v_cmp_lt_i32_e32 vcc, s88, v9
	v_mov_b32_e32 v9, s86
	s_nop 0
	v_cndmask_b32_e32 v8, 8, v2, vcc
	v_mov_b32_e32 v2, s83
	ds_read2_b32 v[2:3], v2 offset1:1
	ds_read2_b32 v[4:5], v4 offset1:1
	ds_read2_b32 v[6:7], v6 offset1:1
	ds_read_b32 v9, v9
	s_waitcnt lgkmcnt(3)
	v_cmp_lt_i32_e32 vcc, s88, v2
	s_nop 1
	v_cndmask_b32_e32 v2, 9, v8, vcc
	v_cmp_lt_i32_e32 vcc, s88, v3
	s_nop 1
	v_cndmask_b32_e32 v2, 10, v2, vcc
	s_waitcnt lgkmcnt(2)
	v_cmp_lt_i32_e32 vcc, s88, v4
	s_nop 1
	v_cndmask_b32_e32 v2, 11, v2, vcc
	v_cmp_lt_i32_e32 vcc, s88, v5
	s_nop 1
	v_cndmask_b32_e32 v2, 12, v2, vcc
	s_waitcnt lgkmcnt(1)
	v_cmp_lt_i32_e32 vcc, s88, v6
	s_nop 1
	v_cndmask_b32_e32 v2, 13, v2, vcc
	v_cmp_lt_i32_e32 vcc, s88, v7
	s_nop 1
	v_cndmask_b32_e32 v2, 14, v2, vcc
	s_waitcnt lgkmcnt(0)
	v_cmp_lt_i32_e32 vcc, s88, v9
	s_nop 1
	v_cndmask_b32_e32 v205, 15, v2, vcc
	v_lshlrev_b32_e32 v2, 2, v205
	v_add_u32_e32 v2, 0, v2
	v_add_u32_e32 v2, 0x20000, v2
	ds_read2_b32 v[2:3], v2 offset1:16
	s_waitcnt lgkmcnt(0)
	v_subrev_u32_e32 v3, s88, v3
	v_lshlrev_b32_e32 v3, 8, v3
	v_add_u32_e32 v206, v3, v2

.LBB0_3327:
	s_or_b64 exec, exec, s[4:5]
	s_add_u32 s54, s40, 0x1a000
	s_addc_u32 s55, s41, 0
	s_add_u32 s24, s0, 0xf8
	s_addc_u32 s25, s1, 0
	s_add_i32 s4, 0, 0x20080
	v_mov_b32_e32 v1, s4
	s_waitcnt lgkmcnt(0)
	s_barrier
	ds_read_b32 v2, v1
	s_load_dword s33, s[0:1], 0xf8
	s_add_u32 s26, s40, 0x300000
	s_addc_u32 s27, s41, 0
	s_add_u32 s12, s40, 0x36600000
	s_waitcnt lgkmcnt(0)
	v_readfirstlane_b32 s35, v2
	v_mov_b32 v2, v0
	ds_read_b32 v1, v1
	s_addc_u32 s4, s41, 0
	s_mov_b32 s97, s2
	s_cmp_lg_u32 s33, 0x100
	s_cbranch_scc1 .Lmoe_perm_done_1
	s_and_b32 s97, s2, 7
	s_lshl_b32 s97, s97, 5
	s_lshr_b32 s98, s2, 6
	s_lshl_b32 s98, s98, 3
	s_or_b32 s97, s97, s98
	s_bfe_u32 s98, s2, 0x30003
	s_or_b32 s97, s97, s98
.Lmoe_perm_done_1:
	s_and_b32 s13, s4, 0xffff
	s_mov_b32 s15, 0x20000
	s_brev_b32 s14, -2
	s_waitcnt lgkmcnt(0)
	v_lshlrev_b32_e32 v1, 3, v1
	v_cmp_ge_i32_e32 vcc, s97, v1
	v_readfirstlane_b32 s6, v2
	s_cbranch_vccnz .LBB0_3386
	v_ashrrev_i32_e32 v1, 31, v2
	v_lshrrev_b32_e32 v1, 26, v1
	v_add_u32_e32 v1, v2, v1
	v_ashrrev_i32_e32 v12, 6, v1
	v_bfe_i32 v1, v2, 27, 1
	v_lshlrev_b32_e32 v3, 4, v2
	v_lshrrev_b32_e32 v1, 22, v1
	v_add_u32_e32 v1, v3, v1
	v_and_b32_e32 v1, 0xfffffc00, v1
	v_sub_u32_e32 v1, v3, v1
	v_lshrrev_b32_e32 v4, 4, v1
	v_bitop3_b32 v13, v4, v1, 32 bitop3:0x6c
	v_ashrrev_i32_e32 v1, 31, v1
	v_lshrrev_b32_e32 v1, 26, v1
	v_lshlrev_b32_e32 v4, 3, v12
	v_add_u32_e32 v1, v13, v1
	v_and_b32_e32 v4, -16, v4
	v_ashrrev_i32_e32 v14, 6, v1
	v_add_u32_e32 v3, 0x2000, v3
	v_add_u32_e32 v1, v14, v4
	v_ashrrev_i32_e32 v4, 31, v3
	v_lshrrev_b32_e32 v4, 22, v4
	v_add_u32_e32 v4, v3, v4
	v_ashrrev_i32_e32 v15, 10, v4
	v_mul_i32_i24_e32 v4, 0x400, v15
	v_sub_u32_e32 v3, v3, v4
	s_add_u32 s16, s40, 0xdc00000
	v_lshrrev_b32_e32 v4, 4, v3
	s_addc_u32 s4, s41, 0
	v_bitop3_b32 v3, v4, v3, 32 bitop3:0x6c
	v_lshlrev_b32_e32 v4, 3, v15
	s_add_u32 s20, s40, 0x4dd00000
	v_and_b32_e32 v16, -16, v4
	v_ashrrev_i32_e32 v4, 31, v3
	s_addc_u32 s5, s41, 0
	v_lshrrev_b32_e32 v4, 26, v4
	s_add_i32 s7, 0, 0x20044
	v_add_u32_e32 v17, v3, v4
	v_mov_b32_e32 v4, s7
	ds_read2_b32 v[4:5], v4 offset1:1
	s_add_i32 s7, 0, 0x2004c
	v_mov_b32_e32 v6, s7
	s_add_i32 s7, 0, 0x20054
	v_mov_b32_e32 v8, s7
	s_add_i32 s7, 0, 0x2005c
	v_mov_b32_e32 v10, s7
	s_ashr_i32 s46, s97, 3
	ds_read2_b32 v[6:7], v6 offset1:1
	ds_read2_b32 v[8:9], v8 offset1:1
	ds_read2_b32 v[10:11], v10 offset1:1
	s_waitcnt lgkmcnt(3)
	v_cmp_ge_i32_e32 vcc, s46, v4
	s_add_i32 s7, 0, 0x20064
	v_add_u32_e32 v197, 0x80, v1
	v_cndmask_b32_e64 v4, 0, 1, vcc
	v_cmp_lt_i32_e32 vcc, s46, v5
	s_mov_b32 s8, 0x1fffe0
	s_and_b32 s17, s4, 0xffff
	v_cndmask_b32_e32 v4, 2, v4, vcc
	s_waitcnt lgkmcnt(2)
	v_cmp_lt_i32_e32 vcc, s46, v6
	s_and_b32 s38, s97, 7
	s_and_b32 s21, s5, 0xffff
	v_cndmask_b32_e32 v4, 3, v4, vcc
	v_cmp_lt_i32_e32 vcc, s46, v7
	s_lshl_b32 s5, s38, 19
	s_mov_b32 s22, s14
	v_cndmask_b32_e32 v4, 4, v4, vcc
	s_waitcnt lgkmcnt(1)
	v_cmp_lt_i32_e32 vcc, s46, v8
	s_mov_b32 s23, s15
	s_mov_b32 s18, s14
	v_cndmask_b32_e32 v4, 5, v4, vcc
	v_cmp_lt_i32_e32 vcc, s46, v9
	s_mov_b32 s19, s15
	s_nop 0
	v_cndmask_b32_e32 v4, 6, v4, vcc
	s_waitcnt lgkmcnt(0)
	v_cmp_lt_i32_e32 vcc, s46, v10
	s_nop 1
	v_cndmask_b32_e32 v4, 7, v4, vcc
	v_cmp_lt_i32_e32 vcc, s46, v11
	s_nop 1
	v_cndmask_b32_e32 v10, 8, v4, vcc
	v_mov_b32_e32 v4, s7
	ds_read2_b32 v[4:5], v4 offset1:1
	s_add_i32 s7, 0, 0x2006c
	v_mov_b32_e32 v6, s7
	s_add_i32 s7, 0, 0x20074
	v_mov_b32_e32 v8, s7
	s_add_i32 s7, 0, 0x2007c
	v_mov_b32_e32 v11, s7
	ds_read2_b32 v[6:7], v6 offset1:1
	ds_read2_b32 v[8:9], v8 offset1:1
	ds_read_b32 v11, v11
	s_waitcnt lgkmcnt(3)
	v_cmp_lt_i32_e32 vcc, s46, v4
	s_movk_i32 s7, 0x4200
	s_nop 0
	v_cndmask_b32_e32 v4, 9, v10, vcc
	v_cmp_lt_i32_e32 vcc, s46, v5
	v_ashrrev_i32_e32 v10, 6, v17
	v_add_u32_e32 v196, v10, v16
	v_cndmask_b32_e32 v4, 10, v4, vcc
	s_waitcnt lgkmcnt(2)
	v_cmp_lt_i32_e32 vcc, s46, v6
	v_add_u32_e32 v198, 0x80, v196
	s_nop 0
	v_cndmask_b32_e32 v4, 11, v4, vcc
	v_cmp_lt_i32_e32 vcc, s46, v7
	s_nop 1
	v_cndmask_b32_e32 v4, 12, v4, vcc
	s_waitcnt lgkmcnt(1)
	v_cmp_lt_i32_e32 vcc, s46, v8
	s_nop 1
	v_cndmask_b32_e32 v4, 13, v4, vcc
	v_cmp_lt_i32_e32 vcc, s46, v9
	s_nop 1
	v_cndmask_b32_e32 v4, 14, v4, vcc
	s_waitcnt lgkmcnt(0)
	v_cmp_lt_i32_e32 vcc, s46, v11
	s_nop 1
	v_cndmask_b32_e32 v194, 15, v4, vcc
	v_lshlrev_b32_e32 v4, 2, v194
	v_add_u32_e32 v4, 0, v4
	v_add_u32_e32 v4, 0x20000, v4
	ds_read2_b32 v[4:5], v4 offset1:16
	v_mul_lo_u32 v11, v194, s7
	s_ashr_i32 s7, s6, 8
	s_waitcnt lgkmcnt(0)
	v_sub_u32_e32 v5, s46, v5
	v_lshlrev_b32_e32 v16, 8, v5
	v_add_u32_e32 v5, v16, v1
	v_add_u32_e32 v18, -1, v4
	v_min_i32_e32 v4, v5, v18
	v_add_u32_e32 v6, v16, v197
	v_add_u32_e32 v8, v16, v196
	v_add_u32_e32 v4, v4, v11
	v_min_i32_e32 v6, v6, v18
	v_min_i32_e32 v8, v8, v18
	v_ashrrev_i32_e32 v5, 31, v4
	v_add_u32_e32 v6, v6, v11
	v_add_u32_e32 v8, v8, v11
	v_lshl_add_u64 v[4:5], v[4:5], 2, s[26:27]
	v_ashrrev_i32_e32 v7, 31, v6
	v_ashrrev_i32_e32 v9, 31, v8
	v_lshl_add_u64 v[6:7], v[6:7], 2, s[26:27]
	v_lshl_add_u64 v[8:9], v[8:9], 2, s[26:27]
	global_load_dword v19, v[4:5], off
	global_load_dword v20, v[6:7], off
	global_load_dword v21, v[8:9], off
	v_add_u32_e32 v4, v16, v198
	v_min_i32_e32 v4, v4, v18
	v_add_u32_e32 v4, v4, v11
	v_ashrrev_i32_e32 v5, 31, v4
	v_lshl_add_u64 v[4:5], v[4:5], 2, s[26:27]
	global_load_dword v4, v[4:5], off
	v_mul_i32_i24_e32 v6, 64, v14
	v_sub_u32_e32 v6, v13, v6
	v_mov_b32_e32 v7, 1
	v_lshlrev_b32_e32 v5, 5, v12
	v_ashrrev_i16_sdwa v6, v7, sext(v6) dst_sel:DWORD dst_unused:UNUSED_PAD src0_sel:DWORD src1_sel:BYTE_0
	v_and_b32_e32 v5, 32, v5
	v_bfe_i32 v6, v6, 0, 16
	v_add_lshl_u32 v199, v5, v6, 1
	v_and_b32_e32 v6, 0xc0, v17
	v_sub_u32_e32 v3, v3, v6
	v_lshlrev_b32_e32 v5, 5, v15
	v_ashrrev_i16_sdwa v3, v7, sext(v3) dst_sel:DWORD dst_unused:UNUSED_PAD src0_sel:DWORD src1_sel:BYTE_0
	v_and_b32_e32 v5, 32, v5
	v_bfe_i32 v3, v3, 0, 16
	v_add_lshl_u32 v201, v5, v3, 1
	v_lshlrev_b32_e32 v8, 1, v1
	v_lshrrev_b32_e32 v9, 2, v1
	v_and_b32_e32 v11, 3, v14
	v_and_b32_e32 v8, 24, v8
	v_and_b32_e32 v9, 4, v9
	v_and_or_b32 v11, v1, s8, v11
	v_or3_b32 v8, v11, v9, v8
	v_lshl_add_u32 v200, v8, 11, v199
	v_and_b32_e32 v8, 3, v10
	v_lshlrev_b32_e32 v6, 1, v196
	v_lshrrev_b32_e32 v7, 2, v196
	v_and_or_b32 v8, v196, s8, v8
	s_ashr_i32 s8, s6, 6
	v_and_b32_e32 v6, 24, v6
	v_and_b32_e32 v7, 4, v7
	s_lshl_b32 s4, s8, 10
	v_or3_b32 v6, v8, v7, v6
	s_add_i32 s47, s4, 0
	v_lshl_add_u32 v202, v6, 11, v201
	s_add_i32 s48, s47, 0x10000
	s_mov_b32 m0, s48
	s_waitcnt vmcnt(3)
	v_lshlrev_b32_e32 v3, 10, v19
	v_and_b32_e32 v3, 0xfffff800, v3
	v_add_u32_e32 v195, v3, v199
	s_waitcnt vmcnt(2)
	v_lshlrev_b32_e32 v3, 10, v20
	v_and_b32_e32 v3, 0xfffff800, v3
	v_add_u32_e32 v218, v3, v199
	s_waitcnt vmcnt(1)
	v_lshlrev_b32_e32 v3, 10, v21
	v_and_b32_e32 v3, 0xfffff800, v3
	v_add_u32_e32 v217, v3, v201
	s_waitcnt vmcnt(0)
	v_lshlrev_b32_e32 v3, 10, v4
	v_and_b32_e32 v3, 0xfffff800, v3
	v_add_u32_e32 v219, v3, v201
	v_lshlrev_b32_e32 v3, 22, v194
	v_or_b32_e32 v220, s5, v3
	s_mov_b64 s[4:5], exec
	v_readfirstlane_b32 s9, v220
	s_nop 4
	buffer_load_dwordx4 v200, s[16:19], s9 offen lds
	s_mov_b64 exec, s[4:5]
	s_add_i32 s49, s47, 0x12000
	s_mov_b64 s[4:5], exec
	s_mov_b32 m0, s49
	s_nop 0
	buffer_load_dwordx4 v202, s[16:19], s9 offen lds
	s_mov_b64 exec, s[4:5]
	s_add_i32 s50, s47, 0x14000
	v_or_b32_e32 v3, 0x40000, v220
	s_mov_b64 s[4:5], exec
	s_mov_b32 m0, s50
	v_readfirstlane_b32 s9, v3
	s_nop 4
	buffer_load_dwordx4 v200, s[16:19], s9 offen lds
	s_mov_b64 exec, s[4:5]
	s_add_i32 s51, s47, 0x16000
	s_mov_b64 s[4:5], exec
	s_mov_b32 m0, s51
	s_nop 0
	buffer_load_dwordx4 v202, s[16:19], s9 offen lds
	s_mov_b64 exec, s[4:5]
	s_mov_b32 m0, s47
	s_add_i32 s52, s47, 0x2000
	buffer_load_dwordx4 v195, s[20:23], 0 offen lds
	s_mov_b32 m0, s52
	s_add_i32 s53, s47, 0x4000
	buffer_load_dwordx4 v217, s[20:23], 0 offen lds
	s_mov_b32 m0, s53
	s_add_i32 s56, s47, 0x6000
	buffer_load_dwordx4 v218, s[20:23], 0 offen lds
	s_mov_b32 m0, s56
	s_cmp_eq_u32 s7, 1
	buffer_load_dwordx4 v219, s[20:23], 0 offen lds
	s_cselect_b64 s[10:11], -1, 0
	s_cmp_lg_u32 s7, 1
	s_cbranch_scc1 .LBB0_3338
	s_barrier

.LBB0_3388:
	s_add_i32 s4, 0, 0x20080
	s_movk_i32 s30, 0x400
	v_mov_b32_e32 v1, s4
	v_mov_b32 v2, v0
	ds_read_b32 v1, v1
	s_mul_i32 s6, s57, s33
	s_add_i32 s6, s6, s97
	s_sub_i32 s7, s6, s56
	v_readfirstlane_b32 s31, v2
	s_waitcnt lgkmcnt(0)
	v_lshlrev_b32_e32 v1, 3, v1
	v_cmp_ge_i32_e32 vcc, s7, v1
	v_cmp_lt_i32_e64 s[4:5], s7, v1
	s_cbranch_vccnz .LBB0_3390
	s_ashr_i32 s34, s7, 3
	s_add_i32 s7, 0, 0x20044
	v_mov_b32_e32 v1, s7
	ds_read2_b32 v[4:5], v1 offset1:1
	s_add_i32 s7, 0, 0x2004c
	v_mov_b32_e32 v1, s7
	s_add_i32 s7, 0, 0x20054
	v_mov_b32_e32 v3, s7
	s_add_i32 s7, 0, 0x2005c
	v_mov_b32_e32 v10, s7
	ds_read2_b32 v[6:7], v1 offset1:1
	ds_read2_b32 v[8:9], v3 offset1:1
	ds_read2_b32 v[10:11], v10 offset1:1
	s_waitcnt lgkmcnt(3)
	v_cmp_ge_i32_e32 vcc, s34, v4
	s_add_i32 s7, 0, 0x20064
	v_mov_b32_e32 v3, s7
	v_cndmask_b32_e64 v1, 0, 1, vcc
	v_cmp_lt_i32_e32 vcc, s34, v5
	ds_read2_b32 v[4:5], v3 offset1:1
	s_add_i32 s7, 0, 0x2006c
	v_cndmask_b32_e32 v1, 2, v1, vcc
	s_waitcnt lgkmcnt(3)
	v_cmp_lt_i32_e32 vcc, s34, v6
	v_mov_b32_e32 v3, s7
	s_add_i32 s7, 0, 0x20074
	v_cndmask_b32_e32 v1, 3, v1, vcc
	v_cmp_lt_i32_e32 vcc, s34, v7
	s_and_b32 s58, s6, 7
	s_nop 0
	v_cndmask_b32_e32 v1, 4, v1, vcc
	s_waitcnt lgkmcnt(2)
	v_cmp_lt_i32_e32 vcc, s34, v8
	v_mov_b32_e32 v8, s7
	s_add_i32 s7, 0, 0x2007c
	v_cndmask_b32_e32 v1, 5, v1, vcc
	v_cmp_lt_i32_e32 vcc, s34, v9
	s_nop 1
	v_cndmask_b32_e32 v1, 6, v1, vcc
	s_waitcnt lgkmcnt(1)
	v_cmp_lt_i32_e32 vcc, s34, v10
	v_mov_b32_e32 v10, s7
	ds_read2_b32 v[6:7], v3 offset1:1
	ds_read2_b32 v[8:9], v8 offset1:1
	ds_read_b32 v3, v10
	v_cndmask_b32_e32 v1, 7, v1, vcc
	v_cmp_lt_i32_e32 vcc, s34, v11
	s_nop 1
	v_cndmask_b32_e32 v1, 8, v1, vcc
	s_waitcnt lgkmcnt(3)
	v_cmp_lt_i32_e32 vcc, s34, v4
	s_nop 1
	v_cndmask_b32_e32 v1, 9, v1, vcc
	v_cmp_lt_i32_e32 vcc, s34, v5
	s_nop 1
	v_cndmask_b32_e32 v1, 10, v1, vcc
	s_waitcnt lgkmcnt(2)
	v_cmp_lt_i32_e32 vcc, s34, v6
	s_nop 1
	v_cndmask_b32_e32 v1, 11, v1, vcc
	v_cmp_lt_i32_e32 vcc, s34, v7
	s_nop 1
	v_cndmask_b32_e32 v1, 12, v1, vcc
	s_waitcnt lgkmcnt(1)
	v_cmp_lt_i32_e32 vcc, s34, v8
	s_nop 1
	v_cndmask_b32_e32 v1, 13, v1, vcc
	v_cmp_lt_i32_e32 vcc, s34, v9
	s_nop 1
	v_cndmask_b32_e32 v1, 14, v1, vcc
	s_waitcnt lgkmcnt(0)
	v_cmp_lt_i32_e32 vcc, s34, v3
	s_nop 1
	v_cndmask_b32_e32 v208, 15, v1, vcc
	v_lshlrev_b32_e32 v1, 2, v208
	v_add_u32_e32 v1, 0, v1
	v_add_u32_e32 v1, 0x20000, v1
	ds_read2_b32 v[4:5], v1 offset1:16
	s_waitcnt lgkmcnt(0)
	v_subrev_u32_e32 v1, s34, v5
	v_lshlrev_b32_e32 v1, 8, v1
	v_add_u32_e32 v1, v1, v4
	s_andn2_b64 vcc, exec, s[4:5]
	s_cbranch_vccz .LBB0_3391
	s_branch .LBB0_3487
